# speedup vs baseline: 1.0493x; 1.0049x over previous
.LBB1_81:
	s_barrier
	s_setprio 2
	s_mov_b32 m0, s37
	v_add_u32_e32 v0, s48, v211
	global_load_lds_dwordx4 v0, s[10:11]
	v_add_u32_e32 v0, s48, v212
	s_mov_b32 m0, s38
	s_nop 0
	global_load_lds_dwordx4 v0, s[10:11]
	s_setprio 0
	s_setprio 2
	v_mbcnt_lo_u32_b32 v248, -1, 0
	v_mbcnt_hi_u32_b32 v248, -1, v248
	v_mul_u32_u24_e32 v251, 57, v248
	v_lshrrev_b32_e32 v251, 9, v251
	v_mul_u32_u24_e32 v252, 9, v251
	v_sub_u32_e32 v252, v248, v252
	v_mul_u32_u24_e32 v253, 11, v252
	v_lshrrev_b32_e32 v253, 5, v253
	v_mul_u32_u24_e32 v254, 3, v253
	v_sub_u32_e32 v254, v252, v254
	v_add_u32_e32 v253, -1, v253
	v_mul_lo_u32 v253, v253, s50
	v_add3_u32 v253, v253, v254, -1
	v_lshlrev_b32_e32 v253, 9, v253
	v_lshl_add_u32 v253, v251, 7, v253
	v_add_u32_e32 v248, s47, v253
	v_add_u32_e32 v249, 0x10000, v206
	v_add_u32_e32 v250, 0x10000, v213
	v_readlane_b32 s3, v248, 1
	s_mov_b32 m0, s39
	s_nop 1
	v_add_u32_e32 v0, s3, v206
	global_load_lds_dwordx4 v0, s[18:19]
	v_add_u32_e32 v0, s3, v213
	s_mov_b32 m0, s40
	s_nop 0
	global_load_lds_dwordx4 v0, s[18:19]
	s_setprio 0
	s_setprio 2
	s_mov_b32 m0, s41
	v_add_u32_e32 v0, s48, v214
	global_load_lds_dwordx4 v0, s[10:11]
	v_add_u32_e32 v0, s48, v215
	s_mov_b32 m0, s42
	s_nop 0
	global_load_lds_dwordx4 v0, s[10:11]
	s_setprio 0
	s_waitcnt vmcnt(6)
	s_add_i32 s3, s47, 0xfe00
	s_lshl_b32 s6, s50, 23
	v_add_u32_e32 v128, s48, v218
	s_mov_b32 s8, 0
	s_movk_i32 s7, 0x180
	s_barrier
.Lk_first:
	ds_read_b128 v[130:133], v219 offset:32768
	ds_read_b128 v[134:137], v219 offset:33792
	ds_read_b128 v[138:141], v219 offset:34816
	ds_read_b128 v[142:145], v219 offset:35840
	ds_read_b128 v[178:181], v219 offset:49152
	ds_read_b128 v[182:185], v219 offset:50176
	ds_read_b128 v[186:189], v219 offset:51200
	ds_read_b128 v[190:193], v219 offset:52224
	ds_read_b128 v[146:149], v220
	ds_read_b128 v[150:153], v220 offset:1024
	ds_read_b128 v[154:157], v221
	ds_read_b128 v[158:161], v221 offset:1024
	ds_read_b128 v[162:165], v222
	ds_read_b128 v[166:169], v222 offset:1024
	ds_read_b128 v[170:173], v223
	ds_read_b128 v[174:177], v223 offset:1024
	s_add_i32 s12, s8, 1
	v_readlane_b32 s9, v248, s12
	s_mov_b32 m0, s43
	s_nop 1
	v_add_u32_e32 v251, s9, v249
	global_load_lds_dwordx4 v251, s[18:19]
	v_add_u32_e32 v251, s9, v250
	s_mov_b32 m0, s44
	s_nop 0
	global_load_lds_dwordx4 v251, s[18:19]
	s_waitcnt vmcnt(8) lgkmcnt(0)
	s_barrier
	s_setprio 1
	v_mfma_f32_16x16x32_f16 v[124:127], v[130:133], v[146:149], 0
	v_mfma_f32_16x16x32_f16 v[120:123], v[138:141], v[146:149], 0
	v_mfma_f32_16x16x32_f16 v[116:119], v[130:133], v[154:157], 0
	v_mfma_f32_16x16x32_f16 v[112:115], v[138:141], v[154:157], 0
	v_mfma_f32_16x16x32_f16 v[108:111], v[130:133], v[162:165], 0
	v_mfma_f32_16x16x32_f16 v[104:107], v[138:141], v[162:165], 0
	v_mfma_f32_16x16x32_f16 v[100:103], v[130:133], v[170:173], 0
	v_mfma_f32_16x16x32_f16 v[96:99], v[138:141], v[170:173], 0
	v_mfma_f32_16x16x32_f16 v[124:127], v[134:137], v[150:153], v[124:127]
	v_mfma_f32_16x16x32_f16 v[120:123], v[142:145], v[150:153], v[120:123]
	v_mfma_f32_16x16x32_f16 v[116:119], v[134:137], v[158:161], v[116:119]
	v_mfma_f32_16x16x32_f16 v[112:115], v[142:145], v[158:161], v[112:115]
	v_mfma_f32_16x16x32_f16 v[108:111], v[134:137], v[166:169], v[108:111]
	v_mfma_f32_16x16x32_f16 v[104:107], v[142:145], v[166:169], v[104:107]
	v_mfma_f32_16x16x32_f16 v[100:103], v[134:137], v[174:177], v[100:103]
	v_mfma_f32_16x16x32_f16 v[96:99], v[142:145], v[174:177], v[96:99]
	v_mfma_f32_16x16x32_f16 v[52:55], v[178:181], v[146:149], 0
	v_mfma_f32_16x16x32_f16 v[40:43], v[186:189], v[146:149], 0
	v_mfma_f32_16x16x32_f16 v[36:39], v[178:181], v[154:157], 0
	v_mfma_f32_16x16x32_f16 v[32:35], v[186:189], v[154:157], 0
	v_mfma_f32_16x16x32_f16 v[28:31], v[178:181], v[162:165], 0
	v_mfma_f32_16x16x32_f16 v[24:27], v[186:189], v[162:165], 0
	v_mfma_f32_16x16x32_f16 v[20:23], v[178:181], v[170:173], 0
	v_mfma_f32_16x16x32_f16 v[16:19], v[186:189], v[170:173], 0
	v_mfma_f32_16x16x32_f16 v[52:55], v[182:185], v[150:153], v[52:55]
	v_mfma_f32_16x16x32_f16 v[40:43], v[190:193], v[150:153], v[40:43]
	v_mfma_f32_16x16x32_f16 v[36:39], v[182:185], v[158:161], v[36:39]
	v_mfma_f32_16x16x32_f16 v[32:35], v[190:193], v[158:161], v[32:35]
	v_mfma_f32_16x16x32_f16 v[28:31], v[182:185], v[166:169], v[28:31]
	v_mfma_f32_16x16x32_f16 v[24:27], v[190:193], v[166:169], v[24:27]
	v_mfma_f32_16x16x32_f16 v[20:23], v[182:185], v[174:177], v[20:23]
	v_mfma_f32_16x16x32_f16 v[16:19], v[190:193], v[174:177], v[16:19]
	s_setprio 0
	s_barrier
	ds_read_b128 v[146:149], v220 offset:16384
	ds_read_b128 v[150:153], v220 offset:17408
	ds_read_b128 v[154:157], v221 offset:16384
	ds_read_b128 v[158:161], v221 offset:17408
	ds_read_b128 v[162:165], v222 offset:16384
	ds_read_b128 v[166:169], v222 offset:17408
	ds_read_b128 v[170:173], v223 offset:16384
	ds_read_b128 v[174:177], v223 offset:17408
	v_add_u32_e32 v129, s7, v128
	s_mov_b32 m0, s22
	v_add_u32_e32 v194, 0xffffff80, v129
	global_load_lds_dwordx4 v194, s[10:11]
	v_add_u32_e32 v194, 0x47f80, v129
	s_mov_b32 m0, s23
	s_add_i32 s9, s8, 2
	global_load_lds_dwordx4 v194, s[10:11]
	v_readlane_b32 s13, v248, s9
	s_mov_b32 m0, s21
	s_nop 1
	v_add_u32_e32 v194, s13, v206
	global_load_lds_dwordx4 v194, s[18:19]
	v_add_u32_e32 v194, s13, v213
	s_mov_b32 m0, s24
	s_nop 0
	global_load_lds_dwordx4 v194, s[18:19]
	s_mov_b32 m0, s25
	v_add_u32_e32 v194, 0x8ff80, v129
	global_load_lds_dwordx4 v194, s[10:11]
	v_add_u32_e32 v194, 0xd7f80, v129
	s_mov_b32 m0, s26
	s_nop 0
	global_load_lds_dwordx4 v194, s[10:11]
	s_waitcnt vmcnt(8) lgkmcnt(0)
	s_barrier
	s_setprio 1
	v_mfma_f32_16x16x32_f16 v[12:15], v[130:133], v[146:149], 0
	v_mfma_f32_16x16x32_f16 v[8:11], v[138:141], v[146:149], 0
	v_mfma_f32_16x16x32_f16 v[4:7], v[130:133], v[154:157], 0
	v_mfma_f32_16x16x32_f16 v[0:3], v[138:141], v[154:157], 0
	v_mfma_f32_16x16x32_f16 v[44:47], v[130:133], v[162:165], 0
	v_mfma_f32_16x16x32_f16 v[48:51], v[138:141], v[162:165], 0
	v_mfma_f32_16x16x32_f16 v[56:59], v[130:133], v[170:173], 0
	v_mfma_f32_16x16x32_f16 v[60:63], v[138:141], v[170:173], 0
	v_mfma_f32_16x16x32_f16 v[12:15], v[134:137], v[150:153], v[12:15]
	v_mfma_f32_16x16x32_f16 v[8:11], v[142:145], v[150:153], v[8:11]
	v_mfma_f32_16x16x32_f16 v[4:7], v[134:137], v[158:161], v[4:7]
	v_mfma_f32_16x16x32_f16 v[0:3], v[142:145], v[158:161], v[0:3]
	v_mfma_f32_16x16x32_f16 v[44:47], v[134:137], v[166:169], v[44:47]
	v_mfma_f32_16x16x32_f16 v[48:51], v[142:145], v[166:169], v[48:51]
	v_mfma_f32_16x16x32_f16 v[56:59], v[134:137], v[174:177], v[56:59]
	v_mfma_f32_16x16x32_f16 v[60:63], v[142:145], v[174:177], v[60:63]
	v_mfma_f32_16x16x32_f16 v[64:67], v[178:181], v[146:149], 0
	v_mfma_f32_16x16x32_f16 v[68:71], v[186:189], v[146:149], 0
	v_mfma_f32_16x16x32_f16 v[72:75], v[178:181], v[154:157], 0
	v_mfma_f32_16x16x32_f16 v[76:79], v[186:189], v[154:157], 0
	v_mfma_f32_16x16x32_f16 v[80:83], v[178:181], v[162:165], 0
	v_mfma_f32_16x16x32_f16 v[84:87], v[186:189], v[162:165], 0
	v_mfma_f32_16x16x32_f16 v[88:91], v[178:181], v[170:173], 0
	v_mfma_f32_16x16x32_f16 v[92:95], v[186:189], v[170:173], 0
	v_mfma_f32_16x16x32_f16 v[64:67], v[182:185], v[150:153], v[64:67]
	v_mfma_f32_16x16x32_f16 v[68:71], v[190:193], v[150:153], v[68:71]
	v_mfma_f32_16x16x32_f16 v[72:75], v[182:185], v[158:161], v[72:75]
	v_mfma_f32_16x16x32_f16 v[76:79], v[190:193], v[158:161], v[76:79]
	v_mfma_f32_16x16x32_f16 v[80:83], v[182:185], v[166:169], v[80:83]
	v_mfma_f32_16x16x32_f16 v[84:87], v[190:193], v[166:169], v[84:87]
	v_mfma_f32_16x16x32_f16 v[88:91], v[182:185], v[174:177], v[88:91]
	v_mfma_f32_16x16x32_f16 v[92:95], v[190:193], v[174:177], v[92:95]
	s_setprio 0
	s_barrier
	ds_read_b128 v[130:133], v224
	ds_read_b128 v[134:137], v224 offset:1024
	ds_read_b128 v[138:141], v224 offset:2048
	ds_read_b128 v[142:145], v224 offset:3072
	ds_read_b128 v[178:181], v229
	ds_read_b128 v[182:185], v229 offset:1024
	ds_read_b128 v[186:189], v229 offset:2048
	ds_read_b128 v[190:193], v229 offset:3072
	ds_read_b128 v[146:149], v225
	ds_read_b128 v[150:153], v225 offset:1024
	ds_read_b128 v[154:157], v226
	ds_read_b128 v[158:161], v226 offset:1024
	ds_read_b128 v[162:165], v227
	ds_read_b128 v[166:169], v227 offset:1024
	ds_read_b128 v[170:173], v228
	ds_read_b128 v[174:177], v228 offset:1024
	v_readlane_b32 s12, v248, s9
	s_mov_b32 m0, s27
	s_nop 1
	v_add_u32_e32 v251, s12, v249
	global_load_lds_dwordx4 v251, s[18:19]
	v_add_u32_e32 v251, s12, v250
	s_mov_b32 m0, s28
	s_nop 0
	global_load_lds_dwordx4 v251, s[18:19]
	s_waitcnt vmcnt(8) lgkmcnt(0)
	s_barrier
	s_setprio 1
	v_mfma_f32_16x16x32_f16 v[124:127], v[130:133], v[146:149], v[124:127]
	v_mfma_f32_16x16x32_f16 v[120:123], v[138:141], v[146:149], v[120:123]
	v_mfma_f32_16x16x32_f16 v[116:119], v[130:133], v[154:157], v[116:119]
	v_mfma_f32_16x16x32_f16 v[112:115], v[138:141], v[154:157], v[112:115]
	v_mfma_f32_16x16x32_f16 v[108:111], v[130:133], v[162:165], v[108:111]
	v_mfma_f32_16x16x32_f16 v[104:107], v[138:141], v[162:165], v[104:107]
	v_mfma_f32_16x16x32_f16 v[100:103], v[130:133], v[170:173], v[100:103]
	v_mfma_f32_16x16x32_f16 v[96:99], v[138:141], v[170:173], v[96:99]
	v_mfma_f32_16x16x32_f16 v[124:127], v[134:137], v[150:153], v[124:127]
	v_mfma_f32_16x16x32_f16 v[120:123], v[142:145], v[150:153], v[120:123]
	v_mfma_f32_16x16x32_f16 v[116:119], v[134:137], v[158:161], v[116:119]
	v_mfma_f32_16x16x32_f16 v[112:115], v[142:145], v[158:161], v[112:115]
	v_mfma_f32_16x16x32_f16 v[108:111], v[134:137], v[166:169], v[108:111]
	v_mfma_f32_16x16x32_f16 v[104:107], v[142:145], v[166:169], v[104:107]
	v_mfma_f32_16x16x32_f16 v[100:103], v[134:137], v[174:177], v[100:103]
	v_mfma_f32_16x16x32_f16 v[96:99], v[142:145], v[174:177], v[96:99]
	v_mfma_f32_16x16x32_f16 v[52:55], v[178:181], v[146:149], v[52:55]
	v_mfma_f32_16x16x32_f16 v[40:43], v[186:189], v[146:149], v[40:43]
	v_mfma_f32_16x16x32_f16 v[36:39], v[178:181], v[154:157], v[36:39]
	v_mfma_f32_16x16x32_f16 v[32:35], v[186:189], v[154:157], v[32:35]
	v_mfma_f32_16x16x32_f16 v[28:31], v[178:181], v[162:165], v[28:31]
	v_mfma_f32_16x16x32_f16 v[24:27], v[186:189], v[162:165], v[24:27]
	v_mfma_f32_16x16x32_f16 v[20:23], v[178:181], v[170:173], v[20:23]
	v_mfma_f32_16x16x32_f16 v[16:19], v[186:189], v[170:173], v[16:19]
	v_mfma_f32_16x16x32_f16 v[52:55], v[182:185], v[150:153], v[52:55]
	v_mfma_f32_16x16x32_f16 v[40:43], v[190:193], v[150:153], v[40:43]
	v_mfma_f32_16x16x32_f16 v[36:39], v[182:185], v[158:161], v[36:39]
	v_mfma_f32_16x16x32_f16 v[32:35], v[190:193], v[158:161], v[32:35]
	v_mfma_f32_16x16x32_f16 v[28:31], v[182:185], v[166:169], v[28:31]
	v_mfma_f32_16x16x32_f16 v[24:27], v[190:193], v[166:169], v[24:27]
	v_mfma_f32_16x16x32_f16 v[20:23], v[182:185], v[174:177], v[20:23]
	v_mfma_f32_16x16x32_f16 v[16:19], v[190:193], v[174:177], v[16:19]
	s_setprio 0
	s_barrier
	ds_read_b128 v[146:149], v230
	ds_read_b128 v[150:153], v230 offset:1024
	ds_read_b128 v[154:157], v231
	ds_read_b128 v[158:161], v231 offset:1024
	ds_read_b128 v[162:165], v232
	ds_read_b128 v[166:169], v232 offset:1024
	ds_read_b128 v[170:173], v233
	ds_read_b128 v[174:177], v233 offset:1024
	s_mov_b32 m0, s37
	v_add_u32_e32 v194, 0x48000, v129
	global_load_lds_dwordx4 v129, s[10:11]
	s_mov_b32 m0, s38
	s_add_i32 s12, s8, 3
	global_load_lds_dwordx4 v194, s[10:11]
	v_readlane_b32 s13, v248, s12
	s_mov_b32 m0, s39
	s_nop 1
	v_add_u32_e32 v194, s13, v206
	global_load_lds_dwordx4 v194, s[18:19]
	v_add_u32_e32 v194, s13, v213
	s_mov_b32 m0, s40
	s_nop 0
	global_load_lds_dwordx4 v194, s[18:19]
	s_mov_b32 m0, s41
	v_add_u32_e32 v194, 0x90000, v129
	global_load_lds_dwordx4 v194, s[10:11]
	v_add_u32_e32 v194, 0xd8000, v129
	s_mov_b32 m0, s42
	s_nop 0
	global_load_lds_dwordx4 v194, s[10:11]
	s_waitcnt vmcnt(8) lgkmcnt(0)
	s_barrier
	s_setprio 1
	v_mfma_f32_16x16x32_f16 v[12:15], v[130:133], v[146:149], v[12:15]
	v_mfma_f32_16x16x32_f16 v[8:11], v[138:141], v[146:149], v[8:11]
	v_mfma_f32_16x16x32_f16 v[4:7], v[130:133], v[154:157], v[4:7]
	v_mfma_f32_16x16x32_f16 v[0:3], v[138:141], v[154:157], v[0:3]
	v_mfma_f32_16x16x32_f16 v[44:47], v[130:133], v[162:165], v[44:47]
	v_mfma_f32_16x16x32_f16 v[48:51], v[138:141], v[162:165], v[48:51]
	v_mfma_f32_16x16x32_f16 v[56:59], v[130:133], v[170:173], v[56:59]
	v_mfma_f32_16x16x32_f16 v[60:63], v[138:141], v[170:173], v[60:63]
	v_mfma_f32_16x16x32_f16 v[12:15], v[134:137], v[150:153], v[12:15]
	v_mfma_f32_16x16x32_f16 v[8:11], v[142:145], v[150:153], v[8:11]
	v_mfma_f32_16x16x32_f16 v[4:7], v[134:137], v[158:161], v[4:7]
	v_mfma_f32_16x16x32_f16 v[0:3], v[142:145], v[158:161], v[0:3]
	v_mfma_f32_16x16x32_f16 v[44:47], v[134:137], v[166:169], v[44:47]
	v_mfma_f32_16x16x32_f16 v[48:51], v[142:145], v[166:169], v[48:51]
	v_mfma_f32_16x16x32_f16 v[56:59], v[134:137], v[174:177], v[56:59]
	v_mfma_f32_16x16x32_f16 v[60:63], v[142:145], v[174:177], v[60:63]
	v_mfma_f32_16x16x32_f16 v[64:67], v[178:181], v[146:149], v[64:67]
	v_mfma_f32_16x16x32_f16 v[68:71], v[186:189], v[146:149], v[68:71]
	v_mfma_f32_16x16x32_f16 v[72:75], v[178:181], v[154:157], v[72:75]
	v_mfma_f32_16x16x32_f16 v[76:79], v[186:189], v[154:157], v[76:79]
	v_mfma_f32_16x16x32_f16 v[80:83], v[178:181], v[162:165], v[80:83]
	v_mfma_f32_16x16x32_f16 v[84:87], v[186:189], v[162:165], v[84:87]
	v_mfma_f32_16x16x32_f16 v[88:91], v[178:181], v[170:173], v[88:91]
	v_mfma_f32_16x16x32_f16 v[92:95], v[186:189], v[170:173], v[92:95]
	v_mfma_f32_16x16x32_f16 v[64:67], v[182:185], v[150:153], v[64:67]
	v_mfma_f32_16x16x32_f16 v[68:71], v[190:193], v[150:153], v[68:71]
	v_mfma_f32_16x16x32_f16 v[72:75], v[182:185], v[158:161], v[72:75]
	v_mfma_f32_16x16x32_f16 v[76:79], v[190:193], v[158:161], v[76:79]
	v_mfma_f32_16x16x32_f16 v[80:83], v[182:185], v[166:169], v[80:83]
	v_mfma_f32_16x16x32_f16 v[84:87], v[190:193], v[166:169], v[84:87]
	v_mfma_f32_16x16x32_f16 v[88:91], v[182:185], v[174:177], v[88:91]
	v_mfma_f32_16x16x32_f16 v[92:95], v[190:193], v[174:177], v[92:95]
	s_setprio 0
	s_addk_i32 s7, 0x100
	s_cmp_lt_u32 s8, 32
	s_mov_b32 s8, s9
	s_barrier
